# GEMM phases: static s_setprio 1 for waves 4-7 over the whole phase (no per-segment flips)
# speedup vs baseline: 1.0203x; 1.0077x over previous
; __device__ __forceinline__ int lt_tid(int wv) { int ln; asm volatile("v_mbcnt_lo_u32_b32 %0, -1, 0\n\tv_mbcnt_hi_u32_b32 %0, -1, %0" : "=v"(ln)); return (wv << 6) | ln; }
;     __device__ __forceinline__ const char* b_ptr(const Unit& u) const { return (const char*)Bt + ((size_t)u.pn * BM * K + u.koff) * 2; }
;     __device__ __forceinline__ const char* b_ptr(const Unit& u) const { return (const char*)Bt + ((size_t)u.e * bstride + (size_t)u.pn * BM * K) * 2; }
; #define PG8_STAGE(bufoff, gbase, voff) do { _Pragma("unroll") for (int _i = 0; _i < 2; ++_i) \
;         __builtin_amdgcn_global_load_lds((const unsigned*)((const char*)(gbase) + (voff)[_i]), (LAS unsigned*)(lds + (bufoff) + ldsw + _i * 8192), 16, 0, 0); } while (0)
; #define PG8_BAR __builtin_amdgcn_s_barrier()
; template <class Epi, class Sched>
; __device__ __forceinline__ void gemm_phase(LAS unsigned char* lds, const bf16_t* Abase, const int K, const Sched& S, const Epi& E, const int wvid) {
;     const int tid = lt_tid(wvid), wid = __builtin_amdgcn_readfirstlane(tid >> 6), lane = tid & 63, wr = wid >> 2, wc = wid & 3, fr = lane & 15, fq = lane >> 4;
;     unsigned voffB[2];
; #pragma unroll
;     for (int i = 0; i < 2; ++i) { int R, C; stage_rc(tid * 16 + i * 8192, R, C); const int Rb = Epi::PERM ? ((R & ~31) + perm32(R & 31)) : R;
;         voffB[i] = (unsigned)(Rb * K + C) * 2u; }
;     const size_t kstep = (size_t)(BK * 2);
;     const size_t hstep = (size_t)HALF * K * 2;
;     const unsigned ldsw = (unsigned)wid * 1024u;
;     const int aoff = lds_byte(wr * 64 + fr, fq * 8), boff = lds_byte(wc * 32 + fr, fq * 8);
;     ...
;     Unit cur, nxt; int ui = 0;
;     if (!S.next(0, cur)) return;
;     f32x4 acc[2][2][4][2];
; #pragma unroll
;     for (int a = 0; a < 2; ++a)
; #pragma unroll
;         for (int b = 0; b < 2; ++b)
; #pragma unroll
;             for (int m = 0; m < 4; ++m)
; #pragma unroll
;                 for (int n = 0; n < 2; ++n) acc[a][b][m][n] = (f32x4){0.f, 0.f, 0.f, 0.f};
;     bf16x8 At[4][2], B0[2][2], B1[2][2];
;     unsigned voffA[2][2];
;     PG8_AOFF(cur);
;     const char* Ab = (const char*)Abase;
;     const char* cB = S.b_ptr(cur);
;     PG8_STAGE(PG8_SB(0, 0), cB, voffB); PG8_STAGE(PG8_SA(0, 0), Ab, voffA[0]); PG8_STAGE(PG8_SB(0, 1), cB + hstep, voffB); PG8_STAGE(PG8_SA(0, 1), Ab, voffA[1]);
;     if (wr == 1) PG8_BAR;
.LBB0_113:
	v_readlane_b32 s2, v254, 52
	v_readlane_b32 s3, v254, 53
	s_xor_b64 s[2:3], s[2:3], -1
	v_writelane_b32 v255, s2, 10
	s_add_u32 s6, s8, 0x13270000
	s_addc_u32 s7, s9, 0
	v_writelane_b32 v255, s3, 11
	s_andn2_b64 vcc, exec, s[0:1]
	s_cbranch_vccnz .LBB0_205
	v_ashrrev_i32_e32 v3, 31, v0
	v_lshrrev_b32_e32 v3, 26, v3
	v_lshlrev_b32_e32 v2, 4, v0
	v_add_u32_e32 v3, v0, v3
	v_bfe_i32 v0, v0, 27, 1
	v_lshrrev_b32_e32 v0, 22, v0
	v_add_u32_e32 v0, v2, v0
	v_and_b32_e32 v0, 0xfffffc00, v0
	v_sub_u32_e32 v0, v2, v0
	v_lshrrev_b32_e32 v4, 4, v0
	v_bitop3_b32 v0, v4, v0, 32 bitop3:0x6c
	v_ashrrev_i32_e32 v5, 31, v0
	v_readlane_b32 s0, v254, 49
	v_ashrrev_i32_e32 v3, 6, v3
	v_lshrrev_b32_e32 v5, 26, v5
	s_mul_i32 s40, s0, 0x2c0000
	v_lshlrev_b32_e32 v4, 3, v3
	v_add_u32_e32 v5, v0, v5
	s_lshl_b64 s[0:1], s[40:41], 1
	v_and_b32_e32 v4, -16, v4
	v_ashrrev_i32_e32 v7, 6, v5
	v_and_b32_e32 v5, 0xc0, v5
	s_add_u32 s38, s6, s0
	v_add_u32_e32 v4, v7, v4
	v_sub_u32_e32 v0, v0, v5
	s_addc_u32 s39, s7, s1
	v_lshlrev_b32_e32 v3, 5, v3
	v_ashrrev_i16_sdwa v0, v216, sext(v0) dst_sel:DWORD dst_unused:UNUSED_PAD src0_sel:DWORD src1_sel:BYTE_0
	v_lshlrev_b32_e32 v5, 1, v4
	s_waitcnt vmcnt(5)
	v_lshrrev_b32_e32 v8, 2, v4
	v_and_b32_e32 v7, 3, v7
	s_mov_b32 s1, 0x1fffe0
	v_and_b32_e32 v3, 32, v3
	v_bfe_i32 v0, v0, 0, 16
	v_and_b32_e32 v5, 24, v5
	v_and_b32_e32 v8, 4, v8
	v_and_or_b32 v4, v4, s1, v7
	v_or3_b32 v4, v4, v8, v5
	v_add_lshl_u32 v0, v3, v0, 1
	v_lshl_add_u32 v178, v4, 11, v0
	v_add_u32_e32 v0, 0x2000, v2
	v_ashrrev_i32_e32 v2, 31, v0
	v_lshrrev_b32_e32 v2, 22, v2
	v_add_u32_e32 v2, v0, v2
	v_ashrrev_i32_e32 v2, 10, v2
	v_mul_i32_i24_e32 v3, 0x400, v2
	v_sub_u32_e32 v0, v0, v3
	v_lshrrev_b32_e32 v3, 4, v0
	v_bitop3_b32 v0, v3, v0, 32 bitop3:0x6c
	v_ashrrev_i32_e32 v4, 31, v0
	v_lshrrev_b32_e32 v4, 26, v4
	v_lshlrev_b32_e32 v3, 3, v2
	v_add_u32_e32 v4, v0, v4
	v_and_b32_e32 v3, -16, v3
	v_ashrrev_i32_e32 v5, 6, v4
	v_and_b32_e32 v4, 0xc0, v4
	v_add_u32_e32 v3, v5, v3
	v_sub_u32_e32 v0, v0, v4
	v_lshlrev_b32_e32 v2, 5, v2
	v_ashrrev_i16_sdwa v0, v216, sext(v0) dst_sel:DWORD dst_unused:UNUSED_PAD src0_sel:DWORD src1_sel:BYTE_0
	v_lshlrev_b32_e32 v4, 1, v3
	v_lshrrev_b32_e32 v7, 2, v3
	v_and_b32_e32 v5, 3, v5
	v_and_b32_e32 v2, 32, v2
	v_bfe_i32 v0, v0, 0, 16
	v_and_b32_e32 v4, 24, v4
	v_and_b32_e32 v7, 4, v7
	v_and_or_b32 v3, v3, s1, v5
	v_or3_b32 v3, v3, v7, v4
	v_add_lshl_u32 v0, v2, v0, 1
	v_lshl_add_u32 v180, v3, 11, v0
	v_mbcnt_lo_u32_b32 v0, -1, 0
	v_mbcnt_hi_u32_b32 v0, -1, v0
	s_add_u32 s10, s8, 0x10000
	v_or_b32_e32 v0, s75, v0
	v_ashrrev_i32_e32 v3, 31, v0
	v_lshrrev_b32_e32 v3, 26, v3
	v_lshlrev_b32_e32 v2, 4, v0
	v_add_u32_e32 v3, v0, v3
	v_bfe_i32 v0, v0, 27, 1
	v_lshrrev_b32_e32 v0, 22, v0
	v_add_u32_e32 v0, v2, v0
	v_and_b32_e32 v0, 0xfffffc00, v0
	v_sub_u32_e32 v0, v2, v0
	v_lshrrev_b32_e32 v4, 4, v0
	v_bitop3_b32 v0, v4, v0, 32 bitop3:0x6c
	v_ashrrev_i32_e32 v5, 31, v0
	v_lshrrev_b32_e32 v5, 26, v5
	v_ashrrev_i32_e32 v3, 6, v3
	v_add_u32_e32 v5, v0, v5
	v_lshlrev_b32_e32 v4, 3, v3
	v_lshrrev_b32_e32 v7, 6, v5
	v_and_b32_e32 v5, 0xc0, v5
	v_and_b32_e32 v4, 0x1ffff0, v4
	v_lshlrev_b32_e32 v3, 5, v3
	v_sub_u32_e32 v0, v0, v5
	v_and_b32_e32 v3, 32, v3
	v_ashrrev_i16_sdwa v0, v216, sext(v0) dst_sel:DWORD dst_unused:UNUSED_PAD src0_sel:DWORD src1_sel:BYTE_0
	v_add_u32_e32 v4, s57, v4
	v_add_u32_sdwa v0, v3, sext(v0) dst_sel:DWORD dst_unused:UNUSED_PAD src0_sel:DWORD src1_sel:WORD_0
	v_add_lshl_u32 v3, v4, v7, 11
	v_add_u32_e32 v2, 0x2000, v2
	v_lshl_add_u32 v0, v0, 1, v3
	v_ashrrev_i32_e32 v3, 31, v2
	v_lshrrev_b32_e32 v3, 22, v3
	v_add_u32_e32 v3, v2, v3
	v_ashrrev_i32_e32 v3, 10, v3
	v_mul_i32_i24_e32 v4, 0x400, v3
	v_sub_u32_e32 v2, v2, v4
	v_lshrrev_b32_e32 v4, 4, v2
	s_addc_u32 s11, s9, 0
	s_ashr_i32 s1, s37, 6
	v_bitop3_b32 v2, v4, v2, 32 bitop3:0x6c
	s_ashr_i32 s17, s16, 31
	s_ashr_i32 s0, s37, 8
	s_lshl_b32 s40, s1, 10
	v_ashrrev_i32_e32 v5, 31, v2
	s_lshl_b64 s[2:3], s[16:17], 19
	v_lshrrev_b32_e32 v5, 26, v5
	s_add_u32 s4, s38, s2
	v_add_u32_e32 v5, v2, v5
	s_addc_u32 s5, s39, s3
	s_add_i32 s17, s40, 0
	v_lshlrev_b32_e32 v4, 3, v3
	v_lshrrev_b32_e32 v7, 6, v5
	v_and_b32_e32 v5, 0xc0, v5
	s_add_i32 s42, s17, 0x10000
	v_and_b32_e32 v4, 0x1ffff0, v4
	v_lshlrev_b32_e32 v3, 5, v3
	v_sub_u32_e32 v2, v2, v5
	s_mov_b32 m0, s42
	s_add_i32 s43, s17, 0x12000
	v_and_b32_e32 v3, 32, v3
	v_ashrrev_i16_sdwa v2, v216, sext(v2) dst_sel:DWORD dst_unused:UNUSED_PAD src0_sel:DWORD src1_sel:BYTE_0
	v_add_u32_e32 v4, s57, v4
	global_load_lds_dwordx4 v178, s[4:5]
	s_mov_b32 m0, s43
	v_add_u32_sdwa v2, v3, sext(v2) dst_sel:DWORD dst_unused:UNUSED_PAD src0_sel:DWORD src1_sel:WORD_0
	v_add_lshl_u32 v3, v4, v7, 11
	global_load_lds_dwordx4 v180, s[4:5]
	s_mov_b32 m0, s17
	s_add_i32 s46, s17, 0x2000
	v_lshl_add_u32 v184, v2, 1, v3
	global_load_lds_dwordx4 v0, s[10:11]
	s_mov_b32 m0, s46
	s_add_u32 s2, s4, 0x40000
	global_load_lds_dwordx4 v184, s[10:11]
	s_addc_u32 s3, s5, 0
	s_add_i32 m0, s17, 0x14000
	s_add_i32 s47, s17, 0x4000
	global_load_lds_dwordx4 v178, s[2:3]
	s_add_i32 m0, s17, 0x16000
	v_add_u32_e32 v182, 0x40000, v0
	global_load_lds_dwordx4 v180, s[2:3]
	s_mov_b32 m0, s47
	s_add_i32 s48, s17, 0x6000
	v_add_u32_e32 v186, 0x40000, v184
	global_load_lds_dwordx4 v182, s[10:11]
	s_mov_b32 m0, s48
	v_mov_b32_e32 v179, v1
	global_load_lds_dwordx4 v186, s[10:11]
	v_mov_b32_e32 v181, v1
	v_lshl_add_u64 v[2:3], s[4:5], 0, v[178:179]
	s_cmp_lg_u32 s0, 1
	v_lshl_add_u64 v[4:5], s[4:5], 0, v[180:181]
	s_cbranch_scc1 .LBB0_116
	s_barrier
	s_setprio 1

; #define PG8_WAIT_V(n) asm volatile("s_waitcnt vmcnt(" #n ")" ::: "memory")
; #define PG8_BAR __builtin_amdgcn_s_barrier()
; template <class Epi, class Sched>
; __device__ __forceinline__ void gemm_phase(LAS unsigned char* lds, const bf16_t* Abase, const int K, const Sched& S, const Epi& E, const int wvid) {
;     ...
;     PG8_WAIT_V(0);
;     if (wr == 0) PG8_BAR;
;     PG8_BAR;
.LBB0_204:
	v_readlane_b32 s34, v254, 54
	s_movk_i32 s35, 0x5700
	s_movk_i32 s38, 0xa00
	s_movk_i32 s39, 0x780
	s_barrier
	s_setprio 0

; __device__ __forceinline__ int lt_tid(int wv) { int ln; asm volatile("v_mbcnt_lo_u32_b32 %0, -1, 0\n\tv_mbcnt_hi_u32_b32 %0, -1, %0" : "=v"(ln)); return (wv << 6) | ln; }
;     __device__ __forceinline__ const char* b_ptr(const Unit& u) const { return (const char*)Bt + ((size_t)u.pn * BM * K + u.koff) * 2; }
;     __device__ __forceinline__ const char* b_ptr(const Unit& u) const { return (const char*)Bt + ((size_t)u.e * bstride + (size_t)u.pn * BM * K) * 2; }
; #define PG8_STAGE(bufoff, gbase, voff) do { _Pragma("unroll") for (int _i = 0; _i < 2; ++_i) \
;         __builtin_amdgcn_global_load_lds((const unsigned*)((const char*)(gbase) + (voff)[_i]), (LAS unsigned*)(lds + (bufoff) + ldsw + _i * 8192), 16, 0, 0); } while (0)
; #define PG8_BAR __builtin_amdgcn_s_barrier()
; template <class Epi, class Sched>
; __device__ __forceinline__ void gemm_phase(LAS unsigned char* lds, const bf16_t* Abase, const int K, const Sched& S, const Epi& E, const int wvid) {
;     const int tid = lt_tid(wvid), wid = __builtin_amdgcn_readfirstlane(tid >> 6), lane = tid & 63, wr = wid >> 2, wc = wid & 3, fr = lane & 15, fq = lane >> 4;
;     unsigned voffB[2];
; #pragma unroll
;     for (int i = 0; i < 2; ++i) { int R, C; stage_rc(tid * 16 + i * 8192, R, C); const int Rb = Epi::PERM ? ((R & ~31) + perm32(R & 31)) : R;
;         voffB[i] = (unsigned)(Rb * K + C) * 2u; }
;     const size_t kstep = (size_t)(BK * 2);
;     const size_t hstep = (size_t)HALF * K * 2;
;     const unsigned ldsw = (unsigned)wid * 1024u;
;     const int aoff = lds_byte(wr * 64 + fr, fq * 8), boff = lds_byte(wc * 32 + fr, fq * 8);
;     ...
;     Unit cur, nxt; int ui = 0;
;     if (!S.next(0, cur)) return;
;     f32x4 acc[2][2][4][2];
; #pragma unroll
;     for (int a = 0; a < 2; ++a)
; #pragma unroll
;         for (int b = 0; b < 2; ++b)
; #pragma unroll
;             for (int m = 0; m < 4; ++m)
; #pragma unroll
;                 for (int n = 0; n < 2; ++n) acc[a][b][m][n] = (f32x4){0.f, 0.f, 0.f, 0.f};
;     bf16x8 At[4][2], B0[2][2], B1[2][2];
;     unsigned voffA[2][2];
;     PG8_AOFF(cur);
;     const char* Ab = (const char*)Abase;
;     const char* cB = S.b_ptr(cur);
;     PG8_STAGE(PG8_SB(0, 0), cB, voffB); PG8_STAGE(PG8_SA(0, 0), Ab, voffA[0]); PG8_STAGE(PG8_SB(0, 1), cB + hstep, voffB); PG8_STAGE(PG8_SA(0, 1), Ab, voffA[1]);
;     if (wr == 1) PG8_BAR;
.LBB0_984:
	v_ashrrev_i32_e32 v3, 31, v0
	v_lshrrev_b32_e32 v3, 26, v3
	v_lshlrev_b32_e32 v2, 4, v0
	v_add_u32_e32 v3, v0, v3
	v_bfe_i32 v0, v0, 27, 1
	v_lshrrev_b32_e32 v0, 22, v0
	v_add_u32_e32 v0, v2, v0
	v_and_b32_e32 v0, 0xfffffc00, v0
	v_sub_u32_e32 v0, v2, v0
	v_lshrrev_b32_e32 v4, 4, v0
	v_bitop3_b32 v0, v4, v0, 32 bitop3:0x6c
	v_ashrrev_i32_e32 v5, 31, v0
	v_ashrrev_i32_e32 v3, 6, v3
	v_lshrrev_b32_e32 v5, 26, v5
	v_lshlrev_b32_e32 v4, 3, v3
	v_add_u32_e32 v5, v0, v5
	v_and_b32_e32 v4, -16, v4
	v_ashrrev_i32_e32 v7, 6, v5
	v_and_b32_e32 v5, 0xc0, v5
	v_add_u32_e32 v4, v7, v4
	v_sub_u32_e32 v0, v0, v5
	v_lshlrev_b32_e32 v3, 5, v3
	v_ashrrev_i16_sdwa v0, v216, sext(v0) dst_sel:DWORD dst_unused:UNUSED_PAD src0_sel:DWORD src1_sel:BYTE_0
	v_lshlrev_b32_e32 v5, 1, v4
	v_lshrrev_b32_e32 v8, 2, v4
	v_and_b32_e32 v7, 3, v7
	s_mov_b32 s5, 0x1fffe0
	v_and_b32_e32 v3, 32, v3
	v_bfe_i32 v0, v0, 0, 16
	v_and_b32_e32 v5, 24, v5
	v_and_b32_e32 v8, 4, v8
	v_and_or_b32 v4, v4, s5, v7
	v_or3_b32 v4, v4, v8, v5
	v_add_lshl_u32 v0, v3, v0, 1
	v_lshl_add_u32 v178, v4, 11, v0
	v_add_u32_e32 v0, 0x2000, v2
	v_ashrrev_i32_e32 v2, 31, v0
	v_lshrrev_b32_e32 v2, 22, v2
	v_add_u32_e32 v2, v0, v2
	v_ashrrev_i32_e32 v2, 10, v2
	v_mul_i32_i24_e32 v3, 0x400, v2
	v_sub_u32_e32 v0, v0, v3
	v_lshrrev_b32_e32 v3, 4, v0
	v_bitop3_b32 v0, v3, v0, 32 bitop3:0x6c
	v_ashrrev_i32_e32 v4, 31, v0
	v_lshrrev_b32_e32 v4, 26, v4
	v_lshlrev_b32_e32 v3, 3, v2
	v_add_u32_e32 v4, v0, v4
	v_and_b32_e32 v3, -16, v3
	v_ashrrev_i32_e32 v5, 6, v4
	v_and_b32_e32 v4, 0xc0, v4
	v_add_u32_e32 v3, v5, v3
	v_sub_u32_e32 v0, v0, v4
	v_lshlrev_b32_e32 v2, 5, v2
	v_ashrrev_i16_sdwa v0, v216, sext(v0) dst_sel:DWORD dst_unused:UNUSED_PAD src0_sel:DWORD src1_sel:BYTE_0
	v_lshlrev_b32_e32 v4, 1, v3
	v_lshrrev_b32_e32 v7, 2, v3
	v_and_b32_e32 v5, 3, v5
	v_and_b32_e32 v2, 32, v2
	v_bfe_i32 v0, v0, 0, 16
	v_and_b32_e32 v4, 24, v4
	v_and_b32_e32 v7, 4, v7
	v_and_or_b32 v3, v3, s5, v5
	v_or3_b32 v3, v3, v7, v4
	v_add_lshl_u32 v0, v2, v0, 1
	v_lshl_add_u32 v180, v3, 11, v0
	v_mbcnt_lo_u32_b32 v0, -1, 0
	v_mbcnt_hi_u32_b32 v0, -1, v0
	s_ashr_i32 s0, s6, 31
	v_or_b32_e32 v0, s75, v0
	v_ashrrev_i32_e32 v3, 31, v0
	v_lshrrev_b32_e32 v3, 26, v3
	s_lshr_b32 s0, s0, 30
	v_lshlrev_b32_e32 v2, 4, v0
	v_add_u32_e32 v3, v0, v3
	v_bfe_i32 v0, v0, 27, 1
	s_add_i32 s6, s6, s0
	v_readlane_b32 s0, v254, 49
	v_lshrrev_b32_e32 v0, 22, v0
	s_ashr_i32 s4, s6, 2
	s_lshl_b32 s0, s0, 21
	v_add_u32_e32 v0, v2, v0
	s_add_u32 s0, s10, s0
	v_and_b32_e32 v0, 0xfffffc00, v0
	s_addc_u32 s1, s11, 0
	v_sub_u32_e32 v0, v2, v0
	s_add_u32 s38, s0, 0x13d70000
	v_lshrrev_b32_e32 v4, 4, v0
	s_addc_u32 s39, s1, 0
	v_bitop3_b32 v0, v4, v0, 32 bitop3:0x6c
	s_add_u32 s0, s10, 0xf1f0000
	v_ashrrev_i32_e32 v5, 31, v0
	s_addc_u32 s1, s11, 0
	s_ashr_i32 s7, s37, 6
	v_lshrrev_b32_e32 v5, 26, v5
	s_ashr_i32 s6, s37, 8
	s_lshl_b32 s40, s7, 10
	s_lshl_b32 s5, s4, 8
	v_ashrrev_i32_e32 v3, 6, v3
	v_add_u32_e32 v5, v0, v5
	s_and_b64 s[16:17], exec, s[2:3]
	v_lshlrev_b32_e32 v4, 3, v3
	v_lshrrev_b32_e32 v7, 6, v5
	v_and_b32_e32 v5, 0xc0, v5
	s_cselect_b32 s16, 0, s5
	v_and_b32_e32 v4, 0x1ffff0, v4
	v_lshlrev_b32_e32 v3, 5, v3
	v_sub_u32_e32 v0, v0, v5
	v_ashrrev_i16_sdwa v0, v216, sext(v0) dst_sel:DWORD dst_unused:UNUSED_PAD src0_sel:DWORD src1_sel:BYTE_0
	v_add_u32_e32 v4, s9, v4
	v_and_or_b32 v3, v3, 32, s16
	v_add_u32_sdwa v0, v3, sext(v0) dst_sel:DWORD dst_unused:UNUSED_PAD src0_sel:DWORD src1_sel:WORD_0
	v_add_lshl_u32 v3, v4, v7, 11
	v_add_u32_e32 v2, 0x2000, v2
	v_lshl_add_u32 v0, v0, 1, v3
	v_ashrrev_i32_e32 v3, 31, v2
	v_lshrrev_b32_e32 v3, 22, v3
	v_add_u32_e32 v3, v2, v3
	v_ashrrev_i32_e32 v3, 10, v3
	v_mul_i32_i24_e32 v4, 0x400, v3
	v_sub_u32_e32 v2, v2, v4
	v_lshrrev_b32_e32 v4, 4, v2
	v_bitop3_b32 v2, v4, v2, 32 bitop3:0x6c
	v_lshlrev_b32_e32 v4, 3, v3
	v_lshlrev_b32_e32 v3, 5, v3
	s_ashr_i32 s23, s22, 31
	s_ashr_i32 s17, s16, 31
	v_and_or_b32 v3, v3, 32, s16
	s_lshl_b64 s[18:19], s[22:23], 19
	s_lshl_b64 s[16:17], s[16:17], 1
	s_add_u32 s5, s38, s18
	v_ashrrev_i32_e32 v5, 31, v2
	s_addc_u32 s8, s39, s19
	v_lshrrev_b32_e32 v5, 26, v5
	s_add_u32 s26, s5, s16
	v_add_u32_e32 v5, v2, v5
	s_addc_u32 s27, s8, s17
	s_add_i32 s42, s40, 0
	v_lshrrev_b32_e32 v7, 6, v5
	v_and_b32_e32 v5, 0xc0, v5
	s_add_i32 s43, s42, 0x10000
	v_and_b32_e32 v4, 0x1ffff0, v4
	v_sub_u32_e32 v2, v2, v5
	s_mov_b32 m0, s43
	s_add_i32 s46, s42, 0x12000
	v_ashrrev_i16_sdwa v2, v216, sext(v2) dst_sel:DWORD dst_unused:UNUSED_PAD src0_sel:DWORD src1_sel:BYTE_0
	v_add_u32_e32 v4, s9, v4
	global_load_lds_dwordx4 v178, s[26:27]
	s_mov_b32 m0, s46
	v_add_u32_sdwa v2, v3, sext(v2) dst_sel:DWORD dst_unused:UNUSED_PAD src0_sel:DWORD src1_sel:WORD_0
	v_add_lshl_u32 v3, v4, v7, 11
	global_load_lds_dwordx4 v180, s[26:27]
	s_mov_b32 m0, s42
	s_add_i32 s47, s42, 0x2000
	v_lshl_add_u32 v184, v2, 1, v3
	global_load_lds_dwordx4 v0, s[0:1]
	s_mov_b32 m0, s47
	s_add_u32 s16, s26, 0x40000
	global_load_lds_dwordx4 v184, s[0:1]
	s_addc_u32 s17, s27, 0
	s_add_i32 m0, s42, 0x14000
	s_add_i32 s48, s42, 0x4000
	global_load_lds_dwordx4 v178, s[16:17]
	s_add_i32 m0, s42, 0x16000
	v_add_u32_e32 v182, 0x40000, v0
	global_load_lds_dwordx4 v180, s[16:17]
	s_mov_b32 m0, s48
	s_add_i32 s49, s42, 0x6000
	v_add_u32_e32 v186, 0x40000, v184
	global_load_lds_dwordx4 v182, s[0:1]
	s_mov_b32 m0, s49
	v_mov_b32_e32 v179, v1
	global_load_lds_dwordx4 v186, s[0:1]
	v_mov_b32_e32 v181, v1
	v_lshl_add_u64 v[2:3], s[26:27], 0, v[178:179]
	s_cmp_lg_u32 s6, 1
	v_lshl_add_u64 v[4:5], s[26:27], 0, v[180:181]
	s_cbranch_scc1 .LBB0_986
	s_barrier
	s_setprio 1

; #define PG8_WAIT_V(n) asm volatile("s_waitcnt vmcnt(" #n ")" ::: "memory")
; #define PG8_BAR __builtin_amdgcn_s_barrier()
; template <class Epi, class Sched>
; __device__ __forceinline__ void gemm_phase(LAS unsigned char* lds, const bf16_t* Abase, const int K, const Sched& S, const Epi& E, const int wvid) {
;     ...
;     PG8_WAIT_V(0);
;     if (wr == 0) PG8_BAR;
;     PG8_BAR;
.LBB0_1013:
	s_barrier
	s_setprio 0

; __device__ __forceinline__ int lt_tid(int wv) { int ln; asm volatile("v_mbcnt_lo_u32_b32 %0, -1, 0\n\tv_mbcnt_hi_u32_b32 %0, -1, %0" : "=v"(ln)); return (wv << 6) | ln; }
;     __device__ __forceinline__ const char* b_ptr(const Unit& u) const { return (const char*)Bt + ((size_t)u.pn * BM * K + u.koff) * 2; }
;     __device__ __forceinline__ const char* b_ptr(const Unit& u) const { return (const char*)Bt + ((size_t)u.e * bstride + (size_t)u.pn * BM * K) * 2; }
; #define PG8_STAGE(bufoff, gbase, voff) do { _Pragma("unroll") for (int _i = 0; _i < 2; ++_i) \
;         __builtin_amdgcn_global_load_lds((const unsigned*)((const char*)(gbase) + (voff)[_i]), (LAS unsigned*)(lds + (bufoff) + ldsw + _i * 8192), 16, 0, 0); } while (0)
; #define PG8_BAR __builtin_amdgcn_s_barrier()
; template <class Epi, class Sched>
; __device__ __forceinline__ void gemm_phase(LAS unsigned char* lds, const bf16_t* Abase, const int K, const Sched& S, const Epi& E, const int wvid) {
;     const int tid = lt_tid(wvid), wid = __builtin_amdgcn_readfirstlane(tid >> 6), lane = tid & 63, wr = wid >> 2, wc = wid & 3, fr = lane & 15, fq = lane >> 4;
;     unsigned voffB[2];
; #pragma unroll
;     for (int i = 0; i < 2; ++i) { int R, C; stage_rc(tid * 16 + i * 8192, R, C); const int Rb = Epi::PERM ? ((R & ~31) + perm32(R & 31)) : R;
;         voffB[i] = (unsigned)(Rb * K + C) * 2u; }
;     const size_t kstep = (size_t)(BK * 2);
;     const size_t hstep = (size_t)HALF * K * 2;
;     const unsigned ldsw = (unsigned)wid * 1024u;
;     const int aoff = lds_byte(wr * 64 + fr, fq * 8), boff = lds_byte(wc * 32 + fr, fq * 8);
;     ...
;     Unit cur, nxt; int ui = 0;
;     if (!S.next(0, cur)) return;
;     f32x4 acc[2][2][4][2];
; #pragma unroll
;     for (int a = 0; a < 2; ++a)
; #pragma unroll
;         for (int b = 0; b < 2; ++b)
; #pragma unroll
;             for (int m = 0; m < 4; ++m)
; #pragma unroll
;                 for (int n = 0; n < 2; ++n) acc[a][b][m][n] = (f32x4){0.f, 0.f, 0.f, 0.f};
;     bf16x8 At[4][2], B0[2][2], B1[2][2];
;     unsigned voffA[2][2];
;     PG8_AOFF(cur);
;     const char* Ab = (const char*)Abase;
;     const char* cB = S.b_ptr(cur);
;     PG8_STAGE(PG8_SB(0, 0), cB, voffB); PG8_STAGE(PG8_SA(0, 0), Ab, voffA[0]); PG8_STAGE(PG8_SB(0, 1), cB + hstep, voffB); PG8_STAGE(PG8_SA(0, 1), Ab, voffA[1]);
;     if (wr == 1) PG8_BAR;
.LBB0_1198:
	v_ashrrev_i32_e32 v7, 31, v6
	v_lshrrev_b32_e32 v7, 26, v7
	v_lshlrev_b32_e32 v0, 4, v6
	v_add_u32_e32 v7, v6, v7
	v_bfe_i32 v6, v6, 27, 1
	v_lshrrev_b32_e32 v6, 22, v6
	v_add_u32_e32 v6, v0, v6
	v_and_b32_e32 v6, 0xfffffc00, v6
	v_sub_u32_e32 v6, v0, v6
	v_lshrrev_b32_e32 v8, 4, v6
	v_bitop3_b32 v6, v8, v6, 32 bitop3:0x6c
	v_ashrrev_i32_e32 v9, 31, v6
	v_ashrrev_i32_e32 v7, 6, v7
	v_lshrrev_b32_e32 v9, 26, v9
	v_lshlrev_b32_e32 v8, 3, v7
	v_add_u32_e32 v9, v6, v9
	v_and_b32_e32 v8, -16, v8
	v_ashrrev_i32_e32 v10, 6, v9
	v_and_b32_e32 v9, 0xc0, v9
	v_add_u32_e32 v8, v10, v8
	v_sub_u32_e32 v6, v6, v9
	v_lshlrev_b32_e32 v7, 5, v7
	v_ashrrev_i16_sdwa v6, v216, sext(v6) dst_sel:DWORD dst_unused:UNUSED_PAD src0_sel:DWORD src1_sel:BYTE_0
	v_lshlrev_b32_e32 v9, 1, v8
	v_lshrrev_b32_e32 v11, 2, v8
	v_and_b32_e32 v10, 3, v10
	s_mov_b32 s1, 0x1fffe0
	v_and_b32_e32 v7, 32, v7
	v_bfe_i32 v6, v6, 0, 16
	v_and_b32_e32 v9, 24, v9
	v_and_b32_e32 v11, 4, v11
	v_and_or_b32 v8, v8, s1, v10
	v_or3_b32 v8, v8, v11, v9
	v_add_lshl_u32 v6, v7, v6, 1
	v_add_u32_e32 v0, 0x2000, v0
	v_lshl_add_u32 v180, v8, 11, v6
	v_ashrrev_i32_e32 v6, 31, v0
	v_lshrrev_b32_e32 v6, 22, v6
	v_add_u32_e32 v6, v0, v6
	v_ashrrev_i32_e32 v6, 10, v6
	v_mul_i32_i24_e32 v7, 0x400, v6
	v_sub_u32_e32 v0, v0, v7
	v_lshrrev_b32_e32 v7, 4, v0
	v_bitop3_b32 v0, v7, v0, 32 bitop3:0x6c
	v_ashrrev_i32_e32 v8, 31, v0
	v_lshrrev_b32_e32 v8, 26, v8
	v_lshlrev_b32_e32 v7, 3, v6
	v_add_u32_e32 v8, v0, v8
	v_and_b32_e32 v7, -16, v7
	v_ashrrev_i32_e32 v9, 6, v8
	v_and_b32_e32 v8, 0xc0, v8
	v_add_u32_e32 v7, v9, v7
	v_sub_u32_e32 v0, v0, v8
	v_lshlrev_b32_e32 v6, 5, v6
	v_ashrrev_i16_sdwa v0, v216, sext(v0) dst_sel:DWORD dst_unused:UNUSED_PAD src0_sel:DWORD src1_sel:BYTE_0
	v_lshlrev_b32_e32 v8, 1, v7
	v_lshrrev_b32_e32 v10, 2, v7
	v_and_b32_e32 v9, 3, v9
	v_and_b32_e32 v6, 32, v6
	v_bfe_i32 v0, v0, 0, 16
	v_and_b32_e32 v8, 24, v8
	v_and_b32_e32 v10, 4, v10
	v_and_or_b32 v7, v7, s1, v9
	v_or3_b32 v7, v7, v10, v8
	v_add_lshl_u32 v0, v6, v0, 1
	v_lshl_add_u32 v182, v7, 11, v0
	v_mbcnt_lo_u32_b32 v0, -1, 0
	v_mbcnt_hi_u32_b32 v0, -1, v0
	v_readlane_b32 s0, v254, 49
	v_or_b32_e32 v0, s75, v0
	v_ashrrev_i32_e32 v6, 31, v0
	v_lshrrev_b32_e32 v6, 26, v6
	v_lshlrev_b32_e32 v8, 4, v0
	v_add_u32_e32 v6, v0, v6
	v_bfe_i32 v0, v0, 27, 1
	v_lshrrev_b32_e32 v0, 22, v0
	v_add_u32_e32 v0, v8, v0
	v_and_b32_e32 v0, 0xfffffc00, v0
	v_sub_u32_e32 v0, v8, v0
	v_lshrrev_b32_e32 v7, 4, v0
	v_bitop3_b32 v0, v7, v0, 32 bitop3:0x6c
	v_ashrrev_i32_e32 v10, 31, v0
	v_ashrrev_i32_e32 v6, 6, v6
	v_lshrrev_b32_e32 v10, 26, v10
	v_lshlrev_b32_e32 v7, 3, v6
	v_add_u32_e32 v10, v0, v10
	v_and_b32_e32 v7, -16, v7
	v_ashrrev_i32_e32 v11, 6, v10
	v_add_u32_e32 v11, v11, v7
	v_and_b32_e32 v7, 0xc0, v10
	v_sub_u32_e32 v0, v0, v7
	v_lshlrev_b32_e32 v6, 5, v6
	v_ashrrev_i16_sdwa v0, v216, sext(v0) dst_sel:DWORD dst_unused:UNUSED_PAD src0_sel:DWORD src1_sel:BYTE_0
	s_lshl_b32 s0, s0, 25
	v_and_b32_e32 v6, 32, v6
	v_bfe_i32 v0, v0, 0, 16
	s_add_u32 s36, s6, s0
	v_add_u32_e32 v9, -1, v179
	v_add_lshl_u32 v10, v6, v0, 1
	v_add_u32_e32 v0, v11, v228
	s_addc_u32 s37, s7, 0
	v_min_i32_e32 v0, v0, v9
	s_add_u32 s10, s8, 0x1a230c00
	v_add_u32_e32 v6, v0, v5
	s_addc_u32 s11, s9, 0
	v_ashrrev_i32_e32 v7, 31, v6
	v_lshl_add_u64 v[6:7], v[6:7], 2, s[10:11]
	v_add_u32_e32 v12, 0x80, v228
	global_load_dword v0, v[6:7], off
	v_add_u32_e32 v6, v11, v12
	v_min_i32_e32 v6, v6, v9
	v_add_u32_e32 v6, v6, v5
	v_ashrrev_i32_e32 v7, 31, v6
	v_lshl_add_u64 v[6:7], v[6:7], 2, s[10:11]
	global_load_dword v6, v[6:7], off
	s_add_u32 s16, s8, 0x10000
	s_addc_u32 s17, s9, 0
	s_ashr_i32 s1, s35, 6
	s_ashr_i32 s25, s24, 31
	s_ashr_i32 s0, s35, 8
	s_lshl_b32 s38, s1, 10
	s_lshl_b64 s[2:3], s[24:25], 19
	s_add_u32 s2, s36, s2
	s_addc_u32 s3, s37, s3
	s_add_i32 s25, s38, 0
	v_lshl_add_u64 v[2:3], s[2:3], 0, v[2:3]
	s_add_i32 s39, s25, 0x10000
	s_mov_b32 m0, s39
	v_readfirstlane_b32 s2, v2
	v_readfirstlane_b32 s3, v3
	s_add_i32 s42, s25, 0x12000
	s_add_i32 s43, s25, 0x2000
	s_add_i32 s46, s25, 0x4000
	s_add_i32 s47, s25, 0x6000
	s_waitcnt vmcnt(1)
	v_lshl_add_u32 v0, v0, 11, v10
	global_load_lds_dwordx4 v180, s[2:3]
	s_mov_b32 m0, s42
	s_waitcnt vmcnt(0)
	v_lshl_add_u32 v186, v6, 11, v10
	v_add_u32_e32 v6, 0x2000, v8
	v_ashrrev_i32_e32 v7, 31, v6
	v_lshrrev_b32_e32 v7, 22, v7
	v_add_u32_e32 v7, v6, v7
	v_ashrrev_i32_e32 v7, 10, v7
	v_mul_i32_i24_e32 v8, 0x400, v7
	v_sub_u32_e32 v6, v6, v8
	v_lshrrev_b32_e32 v8, 4, v6
	v_bitop3_b32 v6, v8, v6, 32 bitop3:0x6c
	v_ashrrev_i32_e32 v10, 31, v6
	v_lshrrev_b32_e32 v10, 26, v10
	v_add_u32_e32 v10, v6, v10
	v_ashrrev_i32_e32 v11, 6, v10
	v_and_b32_e32 v10, 0xc0, v10
	v_lshlrev_b32_e32 v8, 3, v7
	v_sub_u32_e32 v6, v6, v10
	v_and_b32_e32 v8, -16, v8
	v_lshlrev_b32_e32 v7, 5, v7
	v_ashrrev_i16_sdwa v6, v216, sext(v6) dst_sel:DWORD dst_unused:UNUSED_PAD src0_sel:DWORD src1_sel:BYTE_0
	v_add_u32_e32 v8, v11, v8
	v_and_b32_e32 v7, 32, v7
	v_bfe_i32 v6, v6, 0, 16
	v_add_lshl_u32 v10, v7, v6, 1
	v_add_u32_e32 v6, v8, v228
	v_min_i32_e32 v6, v6, v9
	v_add_u32_e32 v6, v6, v5
	v_ashrrev_i32_e32 v7, 31, v6
	v_lshl_add_u64 v[6:7], v[6:7], 2, s[10:11]
	global_load_dword v6, v[6:7], off
	s_waitcnt vmcnt(0)
	v_lshl_add_u32 v184, v6, 11, v10
	v_add_u32_e32 v6, v8, v12
	v_min_i32_e32 v6, v6, v9
	v_add_u32_e32 v6, v6, v5
	v_ashrrev_i32_e32 v7, 31, v6
	v_lshl_add_u64 v[6:7], v[6:7], 2, s[10:11]
	global_load_dword v5, v[6:7], off
	v_lshl_add_u64 v[6:7], v[2:3], 0, s[90:91]
	global_load_lds_dwordx4 v182, s[2:3]
	s_mov_b32 m0, s25
	v_readfirstlane_b32 s2, v6
	global_load_lds_dwordx4 v0, s[16:17]
	s_mov_b32 m0, s43
	v_readfirstlane_b32 s3, v7
	global_load_lds_dwordx4 v184, s[16:17]
	s_add_i32 m0, s25, 0x14000
	s_waitcnt vmcnt(0)
	v_lshl_add_u32 v188, v5, 11, v10
	s_nop 0
	global_load_lds_dwordx4 v180, s[2:3]
	s_add_i32 m0, s25, 0x16000
	s_cmp_lg_u32 s0, 1
	global_load_lds_dwordx4 v182, s[2:3]
	s_mov_b32 m0, s46
	s_nop 0
	global_load_lds_dwordx4 v186, s[16:17]
	s_mov_b32 m0, s47
	s_nop 0
	global_load_lds_dwordx4 v188, s[16:17]
	s_cbranch_scc1 .LBB0_1200
	s_barrier
	s_setprio 1

; #define PG8_WAIT_V(n) asm volatile("s_waitcnt vmcnt(" #n ")" ::: "memory")
; #define PG8_BAR __builtin_amdgcn_s_barrier()
; template <class Epi, class Sched>
; __device__ __forceinline__ void gemm_phase(LAS unsigned char* lds, const bf16_t* Abase, const int K, const Sched& S, const Epi& E, const int wvid) {
;     ...
;     PG8_WAIT_V(0);
;     if (wr == 0) PG8_BAR;
;     PG8_BAR;
; __device__ __forceinline__ void ph_gemm1(const Params& p, int l, LAS unsigned char* lds, const int wvid) {
;     ...
;     if (l == 0) tr_in_tail<2>(p, ws, lds, tab[16] * 4, bid, wvid); else tr_in_tail<5>(p, ws, lds, tab[16] * 4, bid, wvid);
.LBB0_1232:
	v_readlane_b32 s0, v254, 39
	s_barrier
	s_setprio 0
	s_nop 0
	v_mov_b32_e32 v0, s0
	ds_read_b32 v0, v0
	s_waitcnt lgkmcnt(0)
	v_readfirstlane_b32 s0, v0
	s_lshl_b32 s4, s0, 2

; __device__ __forceinline__ int lt_tid(int wv) { int ln; asm volatile("v_mbcnt_lo_u32_b32 %0, -1, 0\n\tv_mbcnt_hi_u32_b32 %0, -1, %0" : "=v"(ln)); return (wv << 6) | ln; }
;     __device__ __forceinline__ const char* b_ptr(const Unit& u) const { return (const char*)Bt + ((size_t)u.pn * BM * K + u.koff) * 2; }
;     __device__ __forceinline__ const char* b_ptr(const Unit& u) const { return (const char*)Bt + ((size_t)u.e * bstride + (size_t)u.pn * BM * K) * 2; }
; #define PG8_STAGE(bufoff, gbase, voff) do { _Pragma("unroll") for (int _i = 0; _i < 2; ++_i) \
;         __builtin_amdgcn_global_load_lds((const unsigned*)((const char*)(gbase) + (voff)[_i]), (LAS unsigned*)(lds + (bufoff) + ldsw + _i * 8192), 16, 0, 0); } while (0)
; #define PG8_BAR __builtin_amdgcn_s_barrier()
; template <class Epi, class Sched>
; __device__ __forceinline__ void gemm_phase(LAS unsigned char* lds, const bf16_t* Abase, const int K, const Sched& S, const Epi& E, const int wvid) {
;     const int tid = lt_tid(wvid), wid = __builtin_amdgcn_readfirstlane(tid >> 6), lane = tid & 63, wr = wid >> 2, wc = wid & 3, fr = lane & 15, fq = lane >> 4;
;     unsigned voffB[2];
; #pragma unroll
;     for (int i = 0; i < 2; ++i) { int R, C; stage_rc(tid * 16 + i * 8192, R, C); const int Rb = Epi::PERM ? ((R & ~31) + perm32(R & 31)) : R;
;         voffB[i] = (unsigned)(Rb * K + C) * 2u; }
;     const size_t kstep = (size_t)(BK * 2);
;     const size_t hstep = (size_t)HALF * K * 2;
;     const unsigned ldsw = (unsigned)wid * 1024u;
;     const int aoff = lds_byte(wr * 64 + fr, fq * 8), boff = lds_byte(wc * 32 + fr, fq * 8);
;     ...
;     Unit cur, nxt; int ui = 0;
;     if (!S.next(0, cur)) return;
;     f32x4 acc[2][2][4][2];
; #pragma unroll
;     for (int a = 0; a < 2; ++a)
; #pragma unroll
;         for (int b = 0; b < 2; ++b)
; #pragma unroll
;             for (int m = 0; m < 4; ++m)
; #pragma unroll
;                 for (int n = 0; n < 2; ++n) acc[a][b][m][n] = (f32x4){0.f, 0.f, 0.f, 0.f};
;     bf16x8 At[4][2], B0[2][2], B1[2][2];
;     unsigned voffA[2][2];
;     PG8_AOFF(cur);
;     const char* Ab = (const char*)Abase;
;     const char* cB = S.b_ptr(cur);
;     PG8_STAGE(PG8_SB(0, 0), cB, voffB); PG8_STAGE(PG8_SA(0, 0), Ab, voffA[0]); PG8_STAGE(PG8_SB(0, 1), cB + hstep, voffB); PG8_STAGE(PG8_SA(0, 1), Ab, voffA[1]);
;     if (wr == 1) PG8_BAR;
.LBB0_1465:
	v_ashrrev_i32_e32 v6, 31, v5
	v_lshrrev_b32_e32 v6, 26, v6
	v_lshlrev_b32_e32 v0, 4, v5
	v_add_u32_e32 v6, v5, v6
	v_bfe_i32 v5, v5, 27, 1
	v_lshrrev_b32_e32 v5, 22, v5
	v_add_u32_e32 v5, v0, v5
	v_and_b32_e32 v5, 0xfffffc00, v5
	v_sub_u32_e32 v5, v0, v5
	v_lshrrev_b32_e32 v7, 4, v5
	v_bitop3_b32 v5, v7, v5, 32 bitop3:0x6c
	v_ashrrev_i32_e32 v8, 31, v5
	v_ashrrev_i32_e32 v6, 6, v6
	v_lshrrev_b32_e32 v8, 26, v8
	v_lshlrev_b32_e32 v7, 3, v6
	v_add_u32_e32 v8, v5, v8
	v_and_b32_e32 v7, -16, v7
	v_ashrrev_i32_e32 v9, 6, v8
	v_and_b32_e32 v8, 0xc0, v8
	v_add_u32_e32 v7, v9, v7
	v_sub_u32_e32 v5, v5, v8
	v_lshlrev_b32_e32 v6, 5, v6
	v_ashrrev_i16_sdwa v5, v216, sext(v5) dst_sel:DWORD dst_unused:UNUSED_PAD src0_sel:DWORD src1_sel:BYTE_0
	v_lshlrev_b32_e32 v8, 1, v7
	v_lshrrev_b32_e32 v10, 2, v7
	v_and_b32_e32 v9, 3, v9
	s_mov_b32 s1, 0x3fffe0
	v_and_b32_e32 v6, 32, v6
	v_bfe_i32 v5, v5, 0, 16
	v_and_b32_e32 v8, 24, v8
	v_and_b32_e32 v10, 4, v10
	v_and_or_b32 v7, v7, s1, v9
	v_or3_b32 v7, v7, v10, v8
	v_add_lshl_u32 v5, v6, v5, 1
	v_add_u32_e32 v0, 0x2000, v0
	v_lshl_add_u32 v180, v7, 10, v5
	v_ashrrev_i32_e32 v5, 31, v0
	v_lshrrev_b32_e32 v5, 22, v5
	v_add_u32_e32 v5, v0, v5
	v_ashrrev_i32_e32 v5, 10, v5
	v_mul_i32_i24_e32 v6, 0x400, v5
	v_sub_u32_e32 v0, v0, v6
	v_lshrrev_b32_e32 v6, 4, v0
	v_bitop3_b32 v0, v6, v0, 32 bitop3:0x6c
	v_ashrrev_i32_e32 v7, 31, v0
	v_lshrrev_b32_e32 v7, 26, v7
	v_lshlrev_b32_e32 v6, 3, v5
	v_add_u32_e32 v7, v0, v7
	v_and_b32_e32 v6, -16, v6
	v_ashrrev_i32_e32 v8, 6, v7
	v_and_b32_e32 v7, 0xc0, v7
	v_add_u32_e32 v6, v8, v6
	v_sub_u32_e32 v0, v0, v7
	v_lshlrev_b32_e32 v5, 5, v5
	v_ashrrev_i16_sdwa v0, v216, sext(v0) dst_sel:DWORD dst_unused:UNUSED_PAD src0_sel:DWORD src1_sel:BYTE_0
	v_lshlrev_b32_e32 v7, 1, v6
	v_lshrrev_b32_e32 v9, 2, v6
	v_and_b32_e32 v8, 3, v8
	v_and_b32_e32 v5, 32, v5
	v_bfe_i32 v0, v0, 0, 16
	v_and_b32_e32 v7, 24, v7
	v_and_b32_e32 v9, 4, v9
	v_and_or_b32 v6, v6, s1, v8
	v_or3_b32 v6, v6, v9, v7
	v_add_lshl_u32 v0, v5, v0, 1
	v_lshl_add_u32 v182, v6, 10, v0
	v_mbcnt_lo_u32_b32 v0, -1, 0
	v_mbcnt_hi_u32_b32 v0, -1, v0
	v_readlane_b32 s0, v254, 49
	v_or_b32_e32 v0, s75, v0
	v_ashrrev_i32_e32 v6, 31, v0
	v_lshrrev_b32_e32 v6, 26, v6
	v_lshlrev_b32_e32 v5, 4, v0
	v_add_u32_e32 v6, v0, v6
	v_bfe_i32 v0, v0, 27, 1
	v_lshrrev_b32_e32 v0, 22, v0
	v_add_u32_e32 v0, v5, v0
	v_and_b32_e32 v0, 0xfffffc00, v0
	v_sub_u32_e32 v0, v5, v0
	v_lshrrev_b32_e32 v7, 4, v0
	v_bitop3_b32 v0, v7, v0, 32 bitop3:0x6c
	v_ashrrev_i32_e32 v8, 31, v0
	v_lshrrev_b32_e32 v8, 26, v8
	v_add_u32_e32 v8, v0, v8
	v_ashrrev_i32_e32 v6, 6, v6
	v_ashrrev_i32_e32 v9, 6, v8
	v_and_b32_e32 v8, 0xc0, v8
	v_lshlrev_b32_e32 v7, 3, v6
	v_sub_u32_e32 v0, v0, v8
	v_and_b32_e32 v7, -16, v7
	v_lshlrev_b32_e32 v6, 5, v6
	v_ashrrev_i16_sdwa v0, v216, sext(v0) dst_sel:DWORD dst_unused:UNUSED_PAD src0_sel:DWORD src1_sel:BYTE_0
	v_add_u32_e32 v7, v9, v7
	v_and_b32_e32 v6, 32, v6
	v_bfe_i32 v0, v0, 0, 16
	v_add_u32_e32 v8, 0x80, v227
	v_add_lshl_u32 v6, v6, v0, 1
	v_add_u32_e32 v0, v7, v227
	v_add_u32_e32 v7, v7, v8
	v_add_u32_e32 v5, 0x2000, v5
	v_lshl_add_u32 v0, v0, 10, v6
	v_lshl_add_u32 v184, v7, 10, v6
	v_ashrrev_i32_e32 v6, 31, v5
	v_lshrrev_b32_e32 v6, 22, v6
	v_add_u32_e32 v6, v5, v6
	v_ashrrev_i32_e32 v6, 10, v6
	v_mul_i32_i24_e32 v7, 0x400, v6
	s_lshl_b32 s0, s0, 24
	v_sub_u32_e32 v5, v5, v7
	s_add_u32 s36, s6, s0
	v_lshrrev_b32_e32 v7, 4, v5
	s_addc_u32 s37, s7, 0
	v_bitop3_b32 v5, v7, v5, 32 bitop3:0x6c
	s_add_u32 s10, s8, 0x4090000
	v_ashrrev_i32_e32 v9, 31, v5
	s_addc_u32 s11, s9, 0
	s_ashr_i32 s1, s35, 6
	v_lshrrev_b32_e32 v9, 26, v9
	s_ashr_i32 s17, s16, 31
	s_ashr_i32 s0, s35, 8
	s_lshl_b32 s38, s1, 10
	v_add_u32_e32 v9, v5, v9
	s_lshl_b64 s[2:3], s[16:17], 18
	v_ashrrev_i32_e32 v10, 6, v9
	v_and_b32_e32 v9, 0xc0, v9
	s_add_u32 s2, s36, s2
	v_lshlrev_b32_e32 v7, 3, v6
	v_sub_u32_e32 v5, v5, v9
	s_addc_u32 s3, s37, s3
	s_add_i32 s17, s38, 0
	v_and_b32_e32 v7, -16, v7
	v_lshlrev_b32_e32 v6, 5, v6
	v_ashrrev_i16_sdwa v5, v216, sext(v5) dst_sel:DWORD dst_unused:UNUSED_PAD src0_sel:DWORD src1_sel:BYTE_0
	v_lshl_add_u64 v[2:3], s[2:3], 0, v[2:3]
	s_add_i32 s39, s17, 0x10000
	v_add_u32_e32 v7, v10, v7
	v_and_b32_e32 v6, 32, v6
	v_bfe_i32 v5, v5, 0, 16
	v_readfirstlane_b32 s2, v2
	v_readfirstlane_b32 s3, v3
	s_mov_b32 m0, s39
	s_add_i32 s42, s17, 0x12000
	v_add_lshl_u32 v5, v6, v5, 1
	v_add_u32_e32 v6, v7, v227
	v_lshl_add_u32 v186, v6, 10, v5
	global_load_lds_dwordx4 v180, s[2:3]
	s_mov_b32 m0, s42
	v_add_u32_e32 v6, v7, v8
	global_load_lds_dwordx4 v182, s[2:3]
	s_mov_b32 m0, s17
	s_add_i32 s43, s17, 0x2000
	v_lshl_add_u32 v188, v6, 10, v5
	global_load_lds_dwordx4 v0, s[10:11]
	s_mov_b32 m0, s43
	v_lshl_add_u64 v[6:7], v[2:3], 0, s[68:69]
	global_load_lds_dwordx4 v186, s[10:11]
	s_add_i32 m0, s17, 0x14000
	v_readfirstlane_b32 s2, v6
	v_readfirstlane_b32 s3, v7
	s_add_i32 s46, s17, 0x4000
	s_add_i32 s47, s17, 0x6000
	s_nop 2
	global_load_lds_dwordx4 v180, s[2:3]
	s_add_i32 m0, s17, 0x16000
	s_cmp_lg_u32 s0, 1
	global_load_lds_dwordx4 v182, s[2:3]
	s_mov_b32 m0, s46
	s_nop 0
	global_load_lds_dwordx4 v184, s[10:11]
	s_mov_b32 m0, s47
	s_nop 0
	global_load_lds_dwordx4 v188, s[10:11]
	s_cbranch_scc1 .LBB0_1467
	s_barrier
	s_setprio 1
